# combo16 + DSA attention: next step's selected-key mask word loaded at the end of the current step (first one before the loop) instead of at the top of its own step
# speedup vs baseline: 1.0064x; 1.0011x over previous
.LBB0_662:
	s_and_b64 vcc, exec, s[10:11]
	s_cbranch_vccz .LBB0_527
	s_mov_b32 s4, s61
	s_waitcnt vmcnt(9)
	v_mbcnt_lo_u32_b32 v40, -1, 0
	v_mbcnt_hi_u32_b32 v40, -1, v40
	s_lshl_b32 s16, s96, 6
	v_lshl_or_b32 v145, s4, 6, v40
	v_ashrrev_i32_e32 v42, 3, v145
	v_readfirstlane_b32 s18, v145
	s_lshr_b32 s4, s18, 2
	s_and_b32 s5, s4, 48
	s_cmp_gt_u32 s96, 3
	s_cselect_b64 s[14:15], -1, 0
	s_add_u32 s12, s51, s21
	s_addc_u32 s13, s64, s20
	s_lshl_b32 s7, s73, 8
	s_lshl_b32 s6, s55, 7
	s_add_u32 s17, s12, s6
	v_and_or_b32 v169, v40, 48, s6
	s_addc_u32 s19, s13, 0
	s_lshl_b32 s6, s82, 2
	s_or_b32 s8, s6, s55
	s_addk_i32 s8, 0x80
	s_ashr_i32 s9, s8, 31
	v_lshrrev_b32_e32 v1, 2, v42
	s_lshl_b64 s[8:9], s[8:9], 18
	v_and_b32_e32 v0, 7, v40
	v_and_b32_e32 v1, 6, v1
	v_bfe_u32 v3, v42, 1, 1
	s_add_u32 s20, s2, s8
	v_lshrrev_b32_e32 v2, 1, v42
	v_bitop3_b32 v0, v1, v0, v3 bitop3:0x36
	s_addc_u32 s21, s3, s9
	s_lshl_b32 s22, s73, 2
	v_lshlrev_b32_e32 v43, 4, v0
	v_xor_b32_e32 v0, v2, v40
	s_or_b32 s10, s22, 3
	v_lshlrev_b32_e32 v41, 4, v0
	v_lshlrev_b32_e32 v0, 1, v40
	v_and_b32_e32 v1, 3, v40
	s_lshl_b32 s8, s10, 6
	s_mul_i32 s9, s10, 0x60000
	v_and_b32_e32 v132, 15, v40
	v_bfe_u32 v137, v40, 4, 2
	s_waitcnt vmcnt(8)
	v_and_or_b32 v44, v0, 24, v1
	v_lshrrev_b32_e32 v0, 1, v40
	v_bfe_u32 v1, v40, 1, 3
	v_lshlrev_b32_e32 v46, 12, v42
	v_mul_lo_u32 v40, v42, s71
	s_mul_hi_u32 s11, s8, 0x1800
	s_add_u32 s8, s17, s9
	v_and_or_b32 v184, v41, s97, v46
	v_or_b32_e32 v40, v43, v40
	s_addc_u32 s9, s19, s11
	v_mov_b32_e32 v41, v185
	v_lshl_add_u64 v[134:135], s[8:9], 0, v[40:41]
	s_lshl_b32 s8, s10, 7
	s_add_u32 s10, s20, s8
	s_addc_u32 s11, s21, 0
	s_or_b32 s9, s22, 2
	v_lshl_add_u64 v[140:141], s[10:11], 0, v[184:185]
	s_lshl_b32 s10, s9, 6
	s_mul_i32 s11, s9, 0x60000
	s_mul_hi_u32 s22, s10, 0x1800
	s_add_u32 s10, s17, s11
	s_addc_u32 s11, s19, s22
	s_lshl_b32 s9, s9, 7
	v_lshl_add_u64 v[138:139], s[10:11], 0, v[40:41]
	s_add_u32 s10, s20, s9
	s_addc_u32 s11, s21, 0
	s_or_b32 s5, s16, s5
	v_lshl_add_u64 v[142:143], s[10:11], 0, v[184:185]
	s_add_u32 s10, s88, s5
	v_mov_b32_e32 v133, v185
	v_lshl_or_b32 v40, v42, 7, v43
	s_addc_u32 s11, s89, 0
	v_lshl_add_u64 v[146:147], s[90:91], 0, v[40:41]
	v_lshl_add_u64 v[40:41], s[10:11], 0, v[132:133]
	v_bitop3_b32 v45, v0, v137, 7 bitop3:0x6c
	v_bitop3_b32 v0, v137, v1, 4 bitop3:0x36
	v_lshlrev_b64 v[40:41], 8, v[40:41]
	s_mov_b64 s[10:11], 0xdc000000
	v_lshl_add_u32 v153, v145, 4, 0
	v_lshlrev_b32_e32 v155, 4, v0
	v_mov_b32_e32 v92, v185
	v_mov_b32_e32 v88, v185
	v_mov_b32_e32 v76, v185
	v_mov_b32_e32 v72, v185
	s_waitcnt vmcnt(4)
	v_mov_b32_e32 v60, v185
	v_mov_b32_e32 v56, v185
	v_mov_b32_e32 v4, v185
	v_mov_b32_e32 v0, v185
	v_lshlrev_b32_e32 v166, 4, v45
	s_waitcnt vmcnt(3)
	v_mov_b32_e32 v64, 0x3f803f80
	v_mov_b32_e32 v167, 0xff800000
	v_mov_b32_e32 v96, v185
	s_waitcnt vmcnt(2)
	v_mov_b32_e32 v68, v185
	v_lshl_add_u32 v170, v44, 7, 0
	v_lshlrev_b32_e32 v136, 3, v137
	v_lshl_add_u64 v[150:151], v[40:41], 0, s[10:11]
	s_waitcnt vmcnt(0)
	v_mov_b64_e32 v[54:55], v[38:39]
	v_mov_b64_e32 v[50:51], v[34:35]
	v_mov_b64_e32 v[46:47], v[30:31]
	v_mov_b64_e32 v[42:43], v[26:27]
	v_mov_b64_e32 v[86:87], v[22:23]
	v_mov_b64_e32 v[82:83], v[18:19]
	s_barrier
	ds_write_b128 v153, v[8:11]
	ds_write_b128 v153, v[12:15] offset:16384
	s_mov_b32 s4, 0
	s_nop 0
	v_mov_b32_e32 v93, v92
	v_mov_b32_e32 v94, v92
	v_mov_b32_e32 v95, v92
	v_mov_b32_e32 v89, v88
	v_mov_b32_e32 v90, v88
	v_mov_b32_e32 v91, v88
	v_mov_b32_e32 v77, v76
	v_mov_b32_e32 v78, v76
	v_mov_b32_e32 v79, v76
	v_mov_b32_e32 v73, v72
	v_mov_b32_e32 v74, v72
	v_mov_b32_e32 v75, v72
	v_mov_b32_e32 v61, v60
	v_mov_b32_e32 v62, v60
	v_mov_b32_e32 v63, v60
	v_mov_b32_e32 v57, v56
	v_mov_b32_e32 v58, v56
	v_mov_b32_e32 v59, v56
	v_lshl_add_u32 v171, v132, 7, 0
	v_mov_b32_e32 v5, v4
	v_mov_b32_e32 v6, v4
	v_mov_b32_e32 v7, v4
	v_mov_b32_e32 v1, v0
	v_mov_b32_e32 v2, v0
	v_mov_b32_e32 v3, v0
	v_mov_b32_e32 v97, v96
	v_mov_b32_e32 v98, v96
	v_mov_b32_e32 v99, v96
	v_mov_b32_e32 v69, v68
	v_mov_b32_e32 v70, v68
	v_mov_b32_e32 v71, v68
	v_mov_b32_e32 v65, v64
	v_mov_b32_e32 v66, v64
	v_mov_b32_e32 v67, v64
	v_or_b32_e32 v172, s7, v132
	v_or_b32_e32 v168, 0x18600, v169
	v_or_b32_e32 v144, 32, v136
	v_lshl_add_u64 v[148:149], s[92:93], 0, v[184:185]
	s_mov_b64 s[16:17], 0
	v_mov_b32_e32 v152, 0
	v_mov_b32_e32 v133, s96
	v_mov_b64_e32 v[52:53], v[36:37]
	v_mov_b64_e32 v[48:49], v[32:33]
	v_mov_b64_e32 v[44:45], v[28:29]
	v_mov_b64_e32 v[40:41], v[24:25]
	v_mov_b32_e32 v174, v167
	v_mov_b32_e32 v175, v167
	v_mov_b32_e32 v154, 0
	v_mov_b64_e32 v[84:85], v[20:21]
	v_mov_b64_e32 v[80:81], v[16:17]
	s_waitcnt lgkmcnt(0)
	s_barrier
	s_andn2_b64 vcc, exec, s[14:15]
	s_nop 0
	s_cbranch_vccnz .Lmsk_pre_skip
	v_lshl_add_u64 v[100:101], s[34:35], 0, v[150:151]
	global_load_dwordx2 v[156:157], v[100:101], off
.Lmsk_pre_skip:
	v_subrev_co_u32_e64 v173, s[10:11], 1, v133
	s_and_b64 s[20:21], s[94:95], s[10:11]
	s_andn2_b64 vcc, exec, s[20:21]
	s_cbranch_vccnz .LBB0_665

.LBB0_665:
	s_andn2_b64 vcc, exec, s[14:15]
	s_nop 0
	s_cbranch_vccz .LBB0_667
	v_mov_b64_e32 v[156:157], -1

.LBB0_678:
	s_waitcnt lgkmcnt(0)
	s_barrier
	v_lshl_add_u64 v[146:147], v[146:147], 0, s[62:63]
	v_lshl_add_u64 v[148:149], v[148:149], 0, s[46:47]
	v_lshl_add_u64 v[150:151], v[150:151], 0, 8
	s_andn2_b64 vcc, exec, s[14:15]
	s_nop 0
	s_cbranch_vccnz .Lmsk_pf_skip
	v_lshl_add_u64 v[100:101], s[34:35], 0, v[150:151]
	global_load_dwordx2 v[156:157], v[100:101], off
.Lmsk_pf_skip:
	s_branch .LBB0_680
.LBB0_679:
	s_cbranch_execnz .LBB0_681
